# v93 + P7 epilogue: the 32 second-branch gate pieces requested together at the start of the epilogue (dead VGPRs) instead of one dependent round trip per piece behind each store
# speedup vs baseline: 1.0136x; 1.0046x over previous
; __device__ __forceinline__ int fresh_lane() { int l; asm volatile("v_mbcnt_lo_u32_b32 %0, -1, 0\n\tv_mbcnt_hi_u32_b32 %0, -1, %0" : "=v"(l)); return l; }
; __device__ __forceinline__ float bf_lo(unsigned w) { return __uint_as_float(w << 16); }
; __device__ __forceinline__ float bf_hi(unsigned w) { return __uint_as_float(w & 0xffff0000u); }
;     __device__ __forceinline__ void operator()(const f32x4 (&acc)[2][2][4][2], const Unit& u, int wr, int wc, int fr_, int fq_) const {
;         const int l_ = fresh_lane(), fr = l_ & 15, fq = l_ >> 4;
;         const int row0 = u.pm * BM + wr * 64 + fr, col0 = u.pn * BM + wc * 32 + 4 * fq;
; #pragma unroll
;         for (int ai = 0; ai < 2; ++ai)
; #pragma unroll
;             for (int m = 0; m < 4; ++m) { const size_t r = (size_t)(row0 + ai * HALF + m * 16);
; #pragma unroll
;                 for (int bj = 0; bj < 2; ++bj)
; #pragma unroll
;                     for (int n = 0; n < 2; ++n) { const u32x2 g = *(const u32x2*)(G + r * ldg + 4096 + col0 + bj * HALF + n * 16); const f32x4 a = acc[ai][bj][m][n];
;                         int w8 = 0; w8 = __builtin_amdgcn_cvt_pk_fp8_f32(16.f * (a[0] * bf_lo(g.x)), 16.f * (a[1] * bf_hi(g.x)), w8, false); w8 = __builtin_amdgcn_cvt_pk_fp8_f32(16.f * (a[2] * bf_lo(g.y)), 16.f * (a[3] * bf_hi(g.y)), w8, true);
;                         *(int*)((unsigned char*)O + r * ldc + col0 + bj * HALF + n * 16) = w8; }
;                 asm volatile("" ::: "memory"); }
.LBB0_2994:
	v_mbcnt_lo_u32_b32 v134, -1, 0
	v_mbcnt_hi_u32_b32 v134, -1, v134
	s_add_i32 s87, s87, s74
	v_and_or_b32 v138, v134, 15, s87
	v_ashrrev_i32_e32 v134, 2, v134
	v_and_b32_e32 v134, -4, v134
	v_add_u32_e32 v134, s43, v134
	v_ashrrev_i32_e32 v139, 31, v138
	v_ashrrev_i32_e32 v135, 31, v134
	v_lshlrev_b64 v[136:137], 14, v[138:139]
	v_lshl_add_u64 v[136:137], s[12:13], 0, v[136:137]
	v_lshlrev_b64 v[140:141], 1, v[134:135]
	v_lshl_add_u64 v[136:137], v[136:137], 0, v[140:141]
	v_add_co_u32_e32 v136, vcc, s66, v136
	v_mov_b32_e32 v144, 0
	s_nop 0
	v_addc_co_u32_e32 v137, vcc, 0, v137, vcc
	v_mov_b32_e32 v220, v138
	v_ashrrev_i32_e32 v221, 31, v220
	v_lshlrev_b64 v[220:221], 14, v[220:221]
	v_lshl_add_u64 v[220:221], s[12:13], 0, v[220:221]
	v_lshl_add_u64 v[220:221], v[220:221], 0, v[140:141]
	v_add_co_u32_e32 v222, vcc, s66, v220
	s_nop 1
	v_addc_co_u32_e32 v223, vcc, 0, v221, vcc
	global_load_dwordx2 v[156:157], v[222:223], off
	global_load_dwordx2 v[158:159], v[222:223], off offset:32
	global_load_dwordx2 v[160:161], v[222:223], off offset:256
	global_load_dwordx2 v[162:163], v[222:223], off offset:288
	v_or_b32_e32 v220, 16, v138
	v_ashrrev_i32_e32 v221, 31, v220
	v_lshlrev_b64 v[220:221], 14, v[220:221]
	v_lshl_add_u64 v[220:221], s[12:13], 0, v[220:221]
	v_lshl_add_u64 v[220:221], v[220:221], 0, v[140:141]
	v_add_co_u32_e32 v222, vcc, s66, v220
	s_nop 1
	v_addc_co_u32_e32 v223, vcc, 0, v221, vcc
	global_load_dwordx2 v[164:165], v[222:223], off
	global_load_dwordx2 v[166:167], v[222:223], off offset:32
	global_load_dwordx2 v[168:169], v[222:223], off offset:256
	global_load_dwordx2 v[170:171], v[222:223], off offset:288
	v_or_b32_e32 v220, 32, v138
	v_ashrrev_i32_e32 v221, 31, v220
	v_lshlrev_b64 v[220:221], 14, v[220:221]
	v_lshl_add_u64 v[220:221], s[12:13], 0, v[220:221]
	v_lshl_add_u64 v[220:221], v[220:221], 0, v[140:141]
	v_add_co_u32_e32 v222, vcc, s66, v220
	s_nop 1
	v_addc_co_u32_e32 v223, vcc, 0, v221, vcc
	global_load_dwordx2 v[172:173], v[222:223], off
	global_load_dwordx2 v[174:175], v[222:223], off offset:32
	global_load_dwordx2 v[176:177], v[222:223], off offset:256
	global_load_dwordx2 v[178:179], v[222:223], off offset:288
	v_or_b32_e32 v220, 48, v138
	v_ashrrev_i32_e32 v221, 31, v220
	v_lshlrev_b64 v[220:221], 14, v[220:221]
	v_lshl_add_u64 v[220:221], s[12:13], 0, v[220:221]
	v_lshl_add_u64 v[220:221], v[220:221], 0, v[140:141]
	v_add_co_u32_e32 v222, vcc, s66, v220
	s_nop 1
	v_addc_co_u32_e32 v223, vcc, 0, v221, vcc
	global_load_dwordx2 v[180:181], v[222:223], off
	global_load_dwordx2 v[182:183], v[222:223], off offset:32
	global_load_dwordx2 v[184:185], v[222:223], off offset:256
	global_load_dwordx2 v[186:187], v[222:223], off offset:288
	v_or_b32_e32 v220, 128, v138
	v_ashrrev_i32_e32 v221, 31, v220
	v_lshlrev_b64 v[220:221], 14, v[220:221]
	v_lshl_add_u64 v[220:221], s[12:13], 0, v[220:221]
	v_lshl_add_u64 v[220:221], v[220:221], 0, v[140:141]
	v_add_co_u32_e32 v222, vcc, s66, v220
	s_nop 1
	v_addc_co_u32_e32 v223, vcc, 0, v221, vcc
	global_load_dwordx2 v[188:189], v[222:223], off
	global_load_dwordx2 v[190:191], v[222:223], off offset:32
	global_load_dwordx2 v[192:193], v[222:223], off offset:256
	global_load_dwordx2 v[194:195], v[222:223], off offset:288
	v_or_b32_e32 v220, 144, v138
	v_ashrrev_i32_e32 v221, 31, v220
	v_lshlrev_b64 v[220:221], 14, v[220:221]
	v_lshl_add_u64 v[220:221], s[12:13], 0, v[220:221]
	v_lshl_add_u64 v[220:221], v[220:221], 0, v[140:141]
	v_add_co_u32_e32 v222, vcc, s66, v220
	s_nop 1
	v_addc_co_u32_e32 v223, vcc, 0, v221, vcc
	global_load_dwordx2 v[196:197], v[222:223], off
	global_load_dwordx2 v[198:199], v[222:223], off offset:32
	global_load_dwordx2 v[200:201], v[222:223], off offset:256
	global_load_dwordx2 v[202:203], v[222:223], off offset:288
	v_or_b32_e32 v220, 160, v138
	v_ashrrev_i32_e32 v221, 31, v220
	v_lshlrev_b64 v[220:221], 14, v[220:221]
	v_lshl_add_u64 v[220:221], s[12:13], 0, v[220:221]
	v_lshl_add_u64 v[220:221], v[220:221], 0, v[140:141]
	v_add_co_u32_e32 v222, vcc, s66, v220
	s_nop 1
	v_addc_co_u32_e32 v223, vcc, 0, v221, vcc
	global_load_dwordx2 v[204:205], v[222:223], off
	global_load_dwordx2 v[206:207], v[222:223], off offset:32
	global_load_dwordx2 v[208:209], v[222:223], off offset:256
	global_load_dwordx2 v[210:211], v[222:223], off offset:288
	v_or_b32_e32 v220, 176, v138
	v_ashrrev_i32_e32 v221, 31, v220
	v_lshlrev_b64 v[220:221], 14, v[220:221]
	v_lshl_add_u64 v[220:221], s[12:13], 0, v[220:221]
	v_lshl_add_u64 v[220:221], v[220:221], 0, v[140:141]
	v_add_co_u32_e32 v222, vcc, s66, v220
	s_nop 1
	v_addc_co_u32_e32 v223, vcc, 0, v221, vcc
	global_load_dwordx2 v[212:213], v[222:223], off
	global_load_dwordx2 v[214:215], v[222:223], off offset:32
	global_load_dwordx2 v[216:217], v[222:223], off offset:256
	global_load_dwordx2 v[218:219], v[222:223], off offset:288
	s_waitcnt vmcnt(31)
	v_mov_b64_e32 v[142:143], v[156:157]
	v_lshlrev_b32_e32 v145, 16, v142
	v_and_b32_e32 v142, 0xffff0000, v142
	v_mul_f32_e32 v126, v126, v145
	v_mul_f32_e32 v127, v127, v142
	v_mul_f32_e32 v126, 0x41800000, v126
	v_mul_f32_e32 v127, 0x41800000, v127
	v_cvt_pk_fp8_f32 v144, v126, v127
	v_lshlrev_b32_e32 v146, 16, v143
	v_and_b32_e32 v143, 0xffff0000, v143
	v_mul_f32_e32 v128, v128, v146
	v_mul_f32_e32 v126, v129, v143
	v_mul_f32_e32 v127, 0x41800000, v128
	v_mul_f32_e32 v126, 0x41800000, v126
	v_cvt_pk_fp8_f32 v144, v127, v126 op_sel:[0,0,1]
	v_lshlrev_b64 v[128:129], 12, v[138:139]
	v_lshl_add_u64 v[126:127], s[14:15], 0, v[134:135]
	v_lshl_add_u64 v[128:129], v[126:127], 0, v[128:129]
	global_store_dword v[128:129], v144, off
	s_waitcnt vmcnt(31)
; __device__ __forceinline__ float bf_lo(unsigned w) { return __uint_as_float(w << 16); }
; __device__ __forceinline__ float bf_hi(unsigned w) { return __uint_as_float(w & 0xffff0000u); }
;     __device__ __forceinline__ void operator()(const f32x4 (&acc)[2][2][4][2], const Unit& u, int wr, int wc, int fr_, int fq_) const {
;     ...
;             for (int m = 0; m < 4; ++m) { const size_t r = (size_t)(row0 + ai * HALF + m * 16);
; #pragma unroll
;                 for (int bj = 0; bj < 2; ++bj)
; #pragma unroll
;                     for (int n = 0; n < 2; ++n) { const u32x2 g = *(const u32x2*)(G + r * ldg + 4096 + col0 + bj * HALF + n * 16); const f32x4 a = acc[ai][bj][m][n];
;                         int w8 = 0; w8 = __builtin_amdgcn_cvt_pk_fp8_f32(16.f * (a[0] * bf_lo(g.x)), 16.f * (a[1] * bf_hi(g.x)), w8, false); w8 = __builtin_amdgcn_cvt_pk_fp8_f32(16.f * (a[2] * bf_lo(g.y)), 16.f * (a[3] * bf_hi(g.y)), w8, true);
;                         *(int*)((unsigned char*)O + r * ldc + col0 + bj * HALF + n * 16) = w8; }
;                 asm volatile("" ::: "memory"); }
	v_mov_b64_e32 v[134:135], v[158:159]
	v_mov_b32_e32 v139, 0
	v_lshlrev_b32_e32 v142, 16, v134
	v_and_b32_e32 v134, 0xffff0000, v134
	v_mul_f32_e32 v122, v122, v142
	v_mul_f32_e32 v123, v123, v134
	v_mul_f32_e32 v122, 0x41800000, v122
	v_mul_f32_e32 v123, 0x41800000, v123
	v_cvt_pk_fp8_f32 v139, v122, v123
	v_lshlrev_b32_e32 v143, 16, v135
	v_and_b32_e32 v135, 0xffff0000, v135
	v_mul_f32_e32 v124, v124, v143
	v_mul_f32_e32 v122, v125, v135
	v_mul_f32_e32 v123, 0x41800000, v124
	v_mul_f32_e32 v122, 0x41800000, v122
	v_cvt_pk_fp8_f32 v139, v123, v122 op_sel:[0,0,1]
	v_mov_b32_e32 v124, 0
	global_store_dword v[128:129], v139, off offset:16
	s_waitcnt vmcnt(31)
	v_mov_b64_e32 v[122:123], v[160:161]
	v_lshlrev_b32_e32 v125, 16, v122
	v_and_b32_e32 v122, 0xffff0000, v122
	v_mul_f32_e32 v118, v118, v125
	v_mul_f32_e32 v119, v119, v122
	v_mul_f32_e32 v118, 0x41800000, v118
	v_mul_f32_e32 v119, 0x41800000, v119
	v_cvt_pk_fp8_f32 v124, v118, v119
	v_lshlrev_b32_e32 v134, 16, v123
	v_and_b32_e32 v123, 0xffff0000, v123
	v_mul_f32_e32 v120, v120, v134
	v_mul_f32_e32 v118, v121, v123
	v_mul_f32_e32 v119, 0x41800000, v120
	v_mul_f32_e32 v118, 0x41800000, v118
	v_cvt_pk_fp8_f32 v124, v119, v118 op_sel:[0,0,1]
	v_or_b32_e32 v120, 16, v138
	v_ashrrev_i32_e32 v121, 31, v120
	v_lshlrev_b64 v[122:123], 14, v[120:121]
	global_store_dword v[128:129], v124, off offset:128
	s_waitcnt vmcnt(31)
	v_mov_b64_e32 v[118:119], v[162:163]
	v_mov_b32_e32 v124, 0
	v_lshl_add_u64 v[122:123], s[12:13], 0, v[122:123]
	v_lshl_add_u64 v[122:123], v[122:123], 0, v[140:141]
	v_lshlrev_b32_e32 v125, 16, v118
	v_and_b32_e32 v118, 0xffff0000, v118
	v_mul_f32_e32 v114, v114, v125
	v_mul_f32_e32 v115, v115, v118
	v_mul_f32_e32 v114, 0x41800000, v114
	v_mul_f32_e32 v115, 0x41800000, v115
	v_cvt_pk_fp8_f32 v124, v114, v115
	v_lshlrev_b32_e32 v134, 16, v119
	v_and_b32_e32 v119, 0xffff0000, v119
	v_mul_f32_e32 v116, v116, v134
	v_mul_f32_e32 v114, v117, v119
	v_mul_f32_e32 v115, 0x41800000, v116
	v_mul_f32_e32 v114, 0x41800000, v114
	v_cvt_pk_fp8_f32 v124, v115, v114 op_sel:[0,0,1]
	v_add_co_u32_e32 v114, vcc, s66, v122
	v_mov_b32_e32 v118, 0
	global_store_dword v[128:129], v124, off offset:144
	v_addc_co_u32_e32 v115, vcc, 0, v123, vcc
	s_waitcnt vmcnt(31)
	v_mov_b64_e32 v[116:117], v[164:165]
	v_lshlrev_b32_e32 v119, 16, v116
	v_and_b32_e32 v116, 0xffff0000, v116
	v_mul_f32_e32 v110, v110, v119
	v_mul_f32_e32 v111, v111, v116
	v_mul_f32_e32 v110, 0x41800000, v110
	v_mul_f32_e32 v111, 0x41800000, v111
	v_cvt_pk_fp8_f32 v118, v110, v111
	v_lshlrev_b32_e32 v122, 16, v117
	v_and_b32_e32 v117, 0xffff0000, v117
	v_mul_f32_e32 v112, v112, v122
	v_mul_f32_e32 v110, v113, v117
	v_mul_f32_e32 v111, 0x41800000, v112
	v_mul_f32_e32 v110, 0x41800000, v110
	v_cvt_pk_fp8_f32 v118, v111, v110 op_sel:[0,0,1]
	v_lshlrev_b64 v[110:111], 12, v[120:121]
	v_lshl_add_u64 v[110:111], v[126:127], 0, v[110:111]
	v_mov_b32_e32 v116, 0
	global_store_dword v[110:111], v118, off
	s_waitcnt vmcnt(31)
	v_mov_b64_e32 v[112:113], v[166:167]
	v_lshlrev_b32_e32 v117, 16, v112
	v_and_b32_e32 v112, 0xffff0000, v112
	v_mul_f32_e32 v106, v106, v117
	v_mul_f32_e32 v107, v107, v112
	v_mul_f32_e32 v106, 0x41800000, v106
	v_mul_f32_e32 v107, 0x41800000, v107
	v_cvt_pk_fp8_f32 v116, v106, v107
	v_lshlrev_b32_e32 v118, 16, v113
	v_and_b32_e32 v113, 0xffff0000, v113
	v_mul_f32_e32 v108, v108, v118
	v_mul_f32_e32 v106, v109, v113
	v_mul_f32_e32 v107, 0x41800000, v108
	v_mul_f32_e32 v106, 0x41800000, v106
	v_cvt_pk_fp8_f32 v116, v107, v106 op_sel:[0,0,1]
	v_mov_b32_e32 v108, 0
	global_store_dword v[110:111], v116, off offset:16
	s_waitcnt vmcnt(31)
	v_mov_b64_e32 v[106:107], v[168:169]
	v_lshlrev_b32_e32 v109, 16, v106
	v_and_b32_e32 v106, 0xffff0000, v106
	v_mul_f32_e32 v102, v102, v109
	v_mul_f32_e32 v103, v103, v106
	v_mul_f32_e32 v102, 0x41800000, v102
	v_mul_f32_e32 v103, 0x41800000, v103
	v_cvt_pk_fp8_f32 v108, v102, v103
	v_lshlrev_b32_e32 v112, 16, v107
	v_and_b32_e32 v107, 0xffff0000, v107
	v_mul_f32_e32 v104, v104, v112
	v_mul_f32_e32 v102, v105, v107
	v_mul_f32_e32 v103, 0x41800000, v104
	v_mul_f32_e32 v102, 0x41800000, v102
	v_cvt_pk_fp8_f32 v108, v103, v102 op_sel:[0,0,1]
	v_or_b32_e32 v104, 32, v138
	v_ashrrev_i32_e32 v105, 31, v104
	v_lshlrev_b64 v[106:107], 14, v[104:105]
	global_store_dword v[110:111], v108, off offset:128
	s_waitcnt vmcnt(31)
	v_mov_b64_e32 v[102:103], v[170:171]
	v_mov_b32_e32 v108, 0
	v_lshl_add_u64 v[106:107], s[12:13], 0, v[106:107]
	v_lshl_add_u64 v[106:107], v[106:107], 0, v[140:141]
	v_lshlrev_b32_e32 v109, 16, v102
	v_and_b32_e32 v102, 0xffff0000, v102
	v_mul_f32_e32 v98, v98, v109
	v_mul_f32_e32 v99, v99, v102
	v_mul_f32_e32 v98, 0x41800000, v98
	v_mul_f32_e32 v99, 0x41800000, v99
	v_cvt_pk_fp8_f32 v108, v98, v99
	v_lshlrev_b32_e32 v112, 16, v103
	v_and_b32_e32 v103, 0xffff0000, v103
	v_mul_f32_e32 v100, v100, v112
	v_mul_f32_e32 v98, v101, v103
	v_mul_f32_e32 v99, 0x41800000, v100
	v_mul_f32_e32 v98, 0x41800000, v98
	v_cvt_pk_fp8_f32 v108, v99, v98 op_sel:[0,0,1]
	v_add_co_u32_e32 v98, vcc, s66, v106
	v_mov_b32_e32 v102, 0
	global_store_dword v[110:111], v108, off offset:144
	v_addc_co_u32_e32 v99, vcc, 0, v107, vcc
	s_waitcnt vmcnt(31)
	v_mov_b64_e32 v[100:101], v[172:173]
	v_lshlrev_b32_e32 v103, 16, v100
	v_and_b32_e32 v100, 0xffff0000, v100
	v_mul_f32_e32 v94, v94, v103
	v_mul_f32_e32 v95, v95, v100
	v_mul_f32_e32 v94, 0x41800000, v94
	v_mul_f32_e32 v95, 0x41800000, v95
	v_cvt_pk_fp8_f32 v102, v94, v95
	v_lshlrev_b32_e32 v106, 16, v101
	v_and_b32_e32 v101, 0xffff0000, v101
	v_mul_f32_e32 v96, v96, v106
	v_mul_f32_e32 v94, v97, v101
	v_mul_f32_e32 v95, 0x41800000, v96
	v_mul_f32_e32 v94, 0x41800000, v94
	v_cvt_pk_fp8_f32 v102, v95, v94 op_sel:[0,0,1]
	v_lshlrev_b64 v[94:95], 12, v[104:105]
	v_lshl_add_u64 v[94:95], v[126:127], 0, v[94:95]
	v_mov_b32_e32 v100, 0
	global_store_dword v[94:95], v102, off
	s_waitcnt vmcnt(31)
; __device__ __forceinline__ float bf_lo(unsigned w) { return __uint_as_float(w << 16); }
; __device__ __forceinline__ float bf_hi(unsigned w) { return __uint_as_float(w & 0xffff0000u); }
;     __device__ __forceinline__ void operator()(const f32x4 (&acc)[2][2][4][2], const Unit& u, int wr, int wc, int fr_, int fq_) const {
;     ...
;             for (int m = 0; m < 4; ++m) { const size_t r = (size_t)(row0 + ai * HALF + m * 16);
; #pragma unroll
;                 for (int bj = 0; bj < 2; ++bj)
; #pragma unroll
;                     for (int n = 0; n < 2; ++n) { const u32x2 g = *(const u32x2*)(G + r * ldg + 4096 + col0 + bj * HALF + n * 16); const f32x4 a = acc[ai][bj][m][n];
;                         int w8 = 0; w8 = __builtin_amdgcn_cvt_pk_fp8_f32(16.f * (a[0] * bf_lo(g.x)), 16.f * (a[1] * bf_hi(g.x)), w8, false); w8 = __builtin_amdgcn_cvt_pk_fp8_f32(16.f * (a[2] * bf_lo(g.y)), 16.f * (a[3] * bf_hi(g.y)), w8, true);
;                         *(int*)((unsigned char*)O + r * ldc + col0 + bj * HALF + n * 16) = w8; }
;                 asm volatile("" ::: "memory"); }
	v_mov_b64_e32 v[96:97], v[174:175]
	v_lshlrev_b32_e32 v101, 16, v96
	v_and_b32_e32 v96, 0xffff0000, v96
	v_mul_f32_e32 v90, v90, v101
	v_mul_f32_e32 v91, v91, v96
	v_mul_f32_e32 v90, 0x41800000, v90
	v_mul_f32_e32 v91, 0x41800000, v91
	v_cvt_pk_fp8_f32 v100, v90, v91
	v_lshlrev_b32_e32 v102, 16, v97
	v_and_b32_e32 v97, 0xffff0000, v97
	v_mul_f32_e32 v92, v92, v102
	v_mul_f32_e32 v90, v93, v97
	v_mul_f32_e32 v91, 0x41800000, v92
	v_mul_f32_e32 v90, 0x41800000, v90
	v_cvt_pk_fp8_f32 v100, v91, v90 op_sel:[0,0,1]
	v_mov_b32_e32 v92, 0
	global_store_dword v[94:95], v100, off offset:16
	s_waitcnt vmcnt(31)
	v_mov_b64_e32 v[90:91], v[176:177]
	v_lshlrev_b32_e32 v93, 16, v90
	v_and_b32_e32 v90, 0xffff0000, v90
	v_mul_f32_e32 v86, v86, v93
	v_mul_f32_e32 v87, v87, v90
	v_mul_f32_e32 v86, 0x41800000, v86
	v_mul_f32_e32 v87, 0x41800000, v87
	v_cvt_pk_fp8_f32 v92, v86, v87
	v_lshlrev_b32_e32 v96, 16, v91
	v_and_b32_e32 v91, 0xffff0000, v91
	v_mul_f32_e32 v88, v88, v96
	v_mul_f32_e32 v86, v89, v91
	v_mul_f32_e32 v87, 0x41800000, v88
	v_mul_f32_e32 v86, 0x41800000, v86
	v_cvt_pk_fp8_f32 v92, v87, v86 op_sel:[0,0,1]
	v_or_b32_e32 v88, 48, v138
	v_ashrrev_i32_e32 v89, 31, v88
	v_lshlrev_b64 v[90:91], 14, v[88:89]
	global_store_dword v[94:95], v92, off offset:128
	s_waitcnt vmcnt(31)
	v_mov_b64_e32 v[86:87], v[178:179]
	v_mov_b32_e32 v92, 0
	v_lshl_add_u64 v[90:91], s[12:13], 0, v[90:91]
	v_lshl_add_u64 v[90:91], v[90:91], 0, v[140:141]
	v_lshlrev_b32_e32 v93, 16, v86
	v_and_b32_e32 v86, 0xffff0000, v86
	v_mul_f32_e32 v82, v82, v93
	v_mul_f32_e32 v83, v83, v86
	v_mul_f32_e32 v82, 0x41800000, v82
	v_mul_f32_e32 v83, 0x41800000, v83
	v_cvt_pk_fp8_f32 v92, v82, v83
	v_lshlrev_b32_e32 v96, 16, v87
	v_and_b32_e32 v87, 0xffff0000, v87
	v_mul_f32_e32 v84, v84, v96
	v_mul_f32_e32 v82, v85, v87
	v_mul_f32_e32 v83, 0x41800000, v84
	v_mul_f32_e32 v82, 0x41800000, v82
	v_cvt_pk_fp8_f32 v92, v83, v82 op_sel:[0,0,1]
	v_add_co_u32_e32 v82, vcc, s66, v90
	v_mov_b32_e32 v86, 0
	global_store_dword v[94:95], v92, off offset:144
	v_addc_co_u32_e32 v83, vcc, 0, v91, vcc
	s_waitcnt vmcnt(31)
	v_mov_b64_e32 v[84:85], v[180:181]
	v_lshlrev_b32_e32 v87, 16, v84
	v_and_b32_e32 v84, 0xffff0000, v84
	v_mul_f32_e32 v78, v78, v87
	v_mul_f32_e32 v79, v79, v84
	v_mul_f32_e32 v78, 0x41800000, v78
	v_mul_f32_e32 v79, 0x41800000, v79
	v_cvt_pk_fp8_f32 v86, v78, v79
	v_lshlrev_b32_e32 v90, 16, v85
	v_and_b32_e32 v85, 0xffff0000, v85
	v_mul_f32_e32 v80, v80, v90
	v_mul_f32_e32 v78, v81, v85
	v_mul_f32_e32 v79, 0x41800000, v80
	v_mul_f32_e32 v78, 0x41800000, v78
	v_cvt_pk_fp8_f32 v86, v79, v78 op_sel:[0,0,1]
	v_lshlrev_b64 v[78:79], 12, v[88:89]
	v_lshl_add_u64 v[78:79], v[126:127], 0, v[78:79]
	v_mov_b32_e32 v84, 0
	global_store_dword v[78:79], v86, off
	s_waitcnt vmcnt(31)
	v_mov_b64_e32 v[80:81], v[182:183]
	v_lshlrev_b32_e32 v85, 16, v80
	v_and_b32_e32 v80, 0xffff0000, v80
	v_mul_f32_e32 v74, v74, v85
	v_mul_f32_e32 v75, v75, v80
	v_mul_f32_e32 v74, 0x41800000, v74
	v_mul_f32_e32 v75, 0x41800000, v75
	v_cvt_pk_fp8_f32 v84, v74, v75
	v_lshlrev_b32_e32 v86, 16, v81
	v_and_b32_e32 v81, 0xffff0000, v81
	v_mul_f32_e32 v76, v76, v86
	v_mul_f32_e32 v74, v77, v81
	v_mul_f32_e32 v75, 0x41800000, v76
	v_mul_f32_e32 v74, 0x41800000, v74
	v_cvt_pk_fp8_f32 v84, v75, v74 op_sel:[0,0,1]
	v_mov_b32_e32 v76, 0
	global_store_dword v[78:79], v84, off offset:16
	s_waitcnt vmcnt(31)
	v_mov_b64_e32 v[74:75], v[184:185]
	v_lshlrev_b32_e32 v77, 16, v74
	v_and_b32_e32 v74, 0xffff0000, v74
	v_mul_f32_e32 v70, v70, v77
	v_mul_f32_e32 v71, v71, v74
	v_mul_f32_e32 v70, 0x41800000, v70
	v_mul_f32_e32 v71, 0x41800000, v71
	v_cvt_pk_fp8_f32 v76, v70, v71
	v_lshlrev_b32_e32 v80, 16, v75
	v_and_b32_e32 v75, 0xffff0000, v75
	v_mul_f32_e32 v72, v72, v80
	v_mul_f32_e32 v70, v73, v75
	v_mul_f32_e32 v71, 0x41800000, v72
	v_mul_f32_e32 v70, 0x41800000, v70
	v_cvt_pk_fp8_f32 v76, v71, v70 op_sel:[0,0,1]
	v_add_u32_e32 v72, 0x80, v138
	v_ashrrev_i32_e32 v73, 31, v72
	v_lshlrev_b64 v[74:75], 14, v[72:73]
	global_store_dword v[78:79], v76, off offset:128
	s_waitcnt vmcnt(31)
	v_mov_b64_e32 v[70:71], v[186:187]
	v_mov_b32_e32 v76, 0
	v_lshl_add_u64 v[74:75], s[12:13], 0, v[74:75]
	v_lshl_add_u64 v[74:75], v[74:75], 0, v[140:141]
	v_lshlrev_b32_e32 v77, 16, v70
	v_and_b32_e32 v70, 0xffff0000, v70
	v_mul_f32_e32 v66, v66, v77
	v_mul_f32_e32 v67, v67, v70
	v_mul_f32_e32 v66, 0x41800000, v66
	v_mul_f32_e32 v67, 0x41800000, v67
	v_cvt_pk_fp8_f32 v76, v66, v67
	v_lshlrev_b32_e32 v80, 16, v71
	v_and_b32_e32 v71, 0xffff0000, v71
	v_mul_f32_e32 v68, v68, v80
	v_mul_f32_e32 v66, v69, v71
	v_mul_f32_e32 v67, 0x41800000, v68
	v_mul_f32_e32 v66, 0x41800000, v66
	v_cvt_pk_fp8_f32 v76, v67, v66 op_sel:[0,0,1]
	v_add_co_u32_e32 v66, vcc, s66, v74
	v_mov_b32_e32 v70, 0
	global_store_dword v[78:79], v76, off offset:144
	v_addc_co_u32_e32 v67, vcc, 0, v75, vcc
	s_waitcnt vmcnt(31)
	v_mov_b64_e32 v[68:69], v[188:189]
	v_lshlrev_b32_e32 v71, 16, v68
	v_and_b32_e32 v68, 0xffff0000, v68
	v_mul_f32_e32 v62, v62, v71
	v_mul_f32_e32 v63, v63, v68
	v_mul_f32_e32 v62, 0x41800000, v62
	v_mul_f32_e32 v63, 0x41800000, v63
	v_cvt_pk_fp8_f32 v70, v62, v63
	v_lshlrev_b32_e32 v74, 16, v69
	v_and_b32_e32 v69, 0xffff0000, v69
	v_mul_f32_e32 v64, v64, v74
	v_mul_f32_e32 v62, v65, v69
	v_mul_f32_e32 v63, 0x41800000, v64
	v_mul_f32_e32 v62, 0x41800000, v62
	v_cvt_pk_fp8_f32 v70, v63, v62 op_sel:[0,0,1]
	v_lshlrev_b64 v[62:63], 12, v[72:73]
	v_lshl_add_u64 v[62:63], v[126:127], 0, v[62:63]
	v_mov_b32_e32 v68, 0
	global_store_dword v[62:63], v70, off
	s_waitcnt vmcnt(31)
; __device__ __forceinline__ float bf_lo(unsigned w) { return __uint_as_float(w << 16); }
; __device__ __forceinline__ float bf_hi(unsigned w) { return __uint_as_float(w & 0xffff0000u); }
;     __device__ __forceinline__ void operator()(const f32x4 (&acc)[2][2][4][2], const Unit& u, int wr, int wc, int fr_, int fq_) const {
;     ...
;             for (int m = 0; m < 4; ++m) { const size_t r = (size_t)(row0 + ai * HALF + m * 16);
; #pragma unroll
;                 for (int bj = 0; bj < 2; ++bj)
; #pragma unroll
;                     for (int n = 0; n < 2; ++n) { const u32x2 g = *(const u32x2*)(G + r * ldg + 4096 + col0 + bj * HALF + n * 16); const f32x4 a = acc[ai][bj][m][n];
;                         int w8 = 0; w8 = __builtin_amdgcn_cvt_pk_fp8_f32(16.f * (a[0] * bf_lo(g.x)), 16.f * (a[1] * bf_hi(g.x)), w8, false); w8 = __builtin_amdgcn_cvt_pk_fp8_f32(16.f * (a[2] * bf_lo(g.y)), 16.f * (a[3] * bf_hi(g.y)), w8, true);
;                         *(int*)((unsigned char*)O + r * ldc + col0 + bj * HALF + n * 16) = w8; }
;                 asm volatile("" ::: "memory"); }
	v_mov_b64_e32 v[64:65], v[190:191]
	v_lshlrev_b32_e32 v69, 16, v64
	v_and_b32_e32 v64, 0xffff0000, v64
	v_mul_f32_e32 v58, v58, v69
	v_mul_f32_e32 v59, v59, v64
	v_mul_f32_e32 v58, 0x41800000, v58
	v_mul_f32_e32 v59, 0x41800000, v59
	v_cvt_pk_fp8_f32 v68, v58, v59
	v_lshlrev_b32_e32 v70, 16, v65
	v_and_b32_e32 v65, 0xffff0000, v65
	v_mul_f32_e32 v60, v60, v70
	v_mul_f32_e32 v58, v61, v65
	v_mul_f32_e32 v59, 0x41800000, v60
	v_mul_f32_e32 v58, 0x41800000, v58
	v_cvt_pk_fp8_f32 v68, v59, v58 op_sel:[0,0,1]
	v_mov_b32_e32 v60, 0
	global_store_dword v[62:63], v68, off offset:16
	s_waitcnt vmcnt(31)
	v_mov_b64_e32 v[58:59], v[192:193]
	v_lshlrev_b32_e32 v61, 16, v58
	v_and_b32_e32 v58, 0xffff0000, v58
	v_mul_f32_e32 v54, v54, v61
	v_mul_f32_e32 v55, v55, v58
	v_mul_f32_e32 v54, 0x41800000, v54
	v_mul_f32_e32 v55, 0x41800000, v55
	v_cvt_pk_fp8_f32 v60, v54, v55
	v_lshlrev_b32_e32 v64, 16, v59
	v_and_b32_e32 v59, 0xffff0000, v59
	v_mul_f32_e32 v56, v56, v64
	v_mul_f32_e32 v54, v57, v59
	v_mul_f32_e32 v55, 0x41800000, v56
	v_mul_f32_e32 v54, 0x41800000, v54
	v_cvt_pk_fp8_f32 v60, v55, v54 op_sel:[0,0,1]
	v_add_u32_e32 v56, 0x90, v138
	v_ashrrev_i32_e32 v57, 31, v56
	v_lshlrev_b64 v[58:59], 14, v[56:57]
	global_store_dword v[62:63], v60, off offset:128
	s_waitcnt vmcnt(31)
	v_mov_b64_e32 v[54:55], v[194:195]
	v_mov_b32_e32 v60, 0
	v_lshl_add_u64 v[58:59], s[12:13], 0, v[58:59]
	v_lshl_add_u64 v[58:59], v[58:59], 0, v[140:141]
	v_lshlrev_b32_e32 v61, 16, v54
	v_and_b32_e32 v54, 0xffff0000, v54
	v_mul_f32_e32 v50, v50, v61
	v_mul_f32_e32 v51, v51, v54
	v_mul_f32_e32 v50, 0x41800000, v50
	v_mul_f32_e32 v51, 0x41800000, v51
	v_cvt_pk_fp8_f32 v60, v50, v51
	v_lshlrev_b32_e32 v64, 16, v55
	v_and_b32_e32 v55, 0xffff0000, v55
	v_mul_f32_e32 v52, v52, v64
	v_mul_f32_e32 v50, v53, v55
	v_mul_f32_e32 v51, 0x41800000, v52
	v_mul_f32_e32 v50, 0x41800000, v50
	v_cvt_pk_fp8_f32 v60, v51, v50 op_sel:[0,0,1]
	v_add_co_u32_e32 v50, vcc, s66, v58
	v_mov_b32_e32 v54, 0
	global_store_dword v[62:63], v60, off offset:144
	v_addc_co_u32_e32 v51, vcc, 0, v59, vcc
	s_waitcnt vmcnt(31)
	v_mov_b64_e32 v[52:53], v[196:197]
	v_lshlrev_b32_e32 v55, 16, v52
	v_and_b32_e32 v52, 0xffff0000, v52
	v_mul_f32_e32 v46, v46, v55
	v_mul_f32_e32 v47, v47, v52
	v_mul_f32_e32 v46, 0x41800000, v46
	v_mul_f32_e32 v47, 0x41800000, v47
	v_cvt_pk_fp8_f32 v54, v46, v47
	v_lshlrev_b32_e32 v58, 16, v53
	v_and_b32_e32 v53, 0xffff0000, v53
	v_mul_f32_e32 v48, v48, v58
	v_mul_f32_e32 v46, v49, v53
	v_mul_f32_e32 v47, 0x41800000, v48
	v_mul_f32_e32 v46, 0x41800000, v46
	v_cvt_pk_fp8_f32 v54, v47, v46 op_sel:[0,0,1]
	v_lshlrev_b64 v[46:47], 12, v[56:57]
	v_lshl_add_u64 v[46:47], v[126:127], 0, v[46:47]
	v_mov_b32_e32 v52, 0
	global_store_dword v[46:47], v54, off
	s_waitcnt vmcnt(31)
	v_mov_b64_e32 v[48:49], v[198:199]
	v_lshlrev_b32_e32 v53, 16, v48
	v_and_b32_e32 v48, 0xffff0000, v48
	v_mul_f32_e32 v42, v42, v53
	v_mul_f32_e32 v43, v43, v48
	v_mul_f32_e32 v42, 0x41800000, v42
	v_mul_f32_e32 v43, 0x41800000, v43
	v_cvt_pk_fp8_f32 v52, v42, v43
	v_lshlrev_b32_e32 v54, 16, v49
	v_and_b32_e32 v49, 0xffff0000, v49
	v_mul_f32_e32 v44, v44, v54
	v_mul_f32_e32 v42, v45, v49
	v_mul_f32_e32 v43, 0x41800000, v44
	v_mul_f32_e32 v42, 0x41800000, v42
	v_cvt_pk_fp8_f32 v52, v43, v42 op_sel:[0,0,1]
	v_mov_b32_e32 v44, 0
	global_store_dword v[46:47], v52, off offset:16
	s_waitcnt vmcnt(31)
	v_mov_b64_e32 v[42:43], v[200:201]
	v_lshlrev_b32_e32 v45, 16, v42
	v_and_b32_e32 v42, 0xffff0000, v42
	v_mul_f32_e32 v38, v38, v45
	v_mul_f32_e32 v39, v39, v42
	v_mul_f32_e32 v38, 0x41800000, v38
	v_mul_f32_e32 v39, 0x41800000, v39
	v_cvt_pk_fp8_f32 v44, v38, v39
	v_lshlrev_b32_e32 v48, 16, v43
	v_and_b32_e32 v43, 0xffff0000, v43
	v_mul_f32_e32 v40, v40, v48
	v_mul_f32_e32 v38, v41, v43
	v_mul_f32_e32 v39, 0x41800000, v40
	v_mul_f32_e32 v38, 0x41800000, v38
	v_cvt_pk_fp8_f32 v44, v39, v38 op_sel:[0,0,1]
	v_add_u32_e32 v40, 0xa0, v138
	v_ashrrev_i32_e32 v41, 31, v40
	v_lshlrev_b64 v[42:43], 14, v[40:41]
	global_store_dword v[46:47], v44, off offset:128
	s_waitcnt vmcnt(31)
	v_mov_b64_e32 v[38:39], v[202:203]
	v_mov_b32_e32 v44, 0
	v_lshl_add_u64 v[42:43], s[12:13], 0, v[42:43]
	v_lshl_add_u64 v[42:43], v[42:43], 0, v[140:141]
	v_lshlrev_b32_e32 v45, 16, v38
	v_and_b32_e32 v38, 0xffff0000, v38
	v_mul_f32_e32 v34, v34, v45
	v_mul_f32_e32 v35, v35, v38
	v_mul_f32_e32 v34, 0x41800000, v34
	v_mul_f32_e32 v35, 0x41800000, v35
	v_cvt_pk_fp8_f32 v44, v34, v35
	v_lshlrev_b32_e32 v48, 16, v39
	v_and_b32_e32 v39, 0xffff0000, v39
	v_mul_f32_e32 v36, v36, v48
	v_mul_f32_e32 v34, v37, v39
	v_mul_f32_e32 v35, 0x41800000, v36
	v_mul_f32_e32 v34, 0x41800000, v34
	v_cvt_pk_fp8_f32 v44, v35, v34 op_sel:[0,0,1]
	v_add_co_u32_e32 v34, vcc, s66, v42
	v_mov_b32_e32 v38, 0
	global_store_dword v[46:47], v44, off offset:144
	v_addc_co_u32_e32 v35, vcc, 0, v43, vcc
	s_waitcnt vmcnt(31)
; __device__ __forceinline__ float bf_lo(unsigned w) { return __uint_as_float(w << 16); }
; __device__ __forceinline__ float bf_hi(unsigned w) { return __uint_as_float(w & 0xffff0000u); }
; #define PG8_BAR __builtin_amdgcn_s_barrier()
;     __device__ __forceinline__ void operator()(const f32x4 (&acc)[2][2][4][2], const Unit& u, int wr, int wc, int fr_, int fq_) const {
;     ...
;             for (int m = 0; m < 4; ++m) { const size_t r = (size_t)(row0 + ai * HALF + m * 16);
; #pragma unroll
;                 for (int bj = 0; bj < 2; ++bj)
; #pragma unroll
;                     for (int n = 0; n < 2; ++n) { const u32x2 g = *(const u32x2*)(G + r * ldg + 4096 + col0 + bj * HALF + n * 16); const f32x4 a = acc[ai][bj][m][n];
;                         int w8 = 0; w8 = __builtin_amdgcn_cvt_pk_fp8_f32(16.f * (a[0] * bf_lo(g.x)), 16.f * (a[1] * bf_hi(g.x)), w8, false); w8 = __builtin_amdgcn_cvt_pk_fp8_f32(16.f * (a[2] * bf_lo(g.y)), 16.f * (a[3] * bf_hi(g.y)), w8, true);
;                         *(int*)((unsigned char*)O + r * ldc + col0 + bj * HALF + n * 16) = w8; }
;                 asm volatile("" ::: "memory"); }
;     ...
;         if constexpr (!Epi::AFTER_DRAIN) { E(acc, cur, wr, wc, fr, fq); S.done(cur); }
;         if (!has_next) break;
; #pragma unroll
;         for (int a = 0; a < 2; ++a)
; #pragma unroll
;             for (int b = 0; b < 2; ++b)
; #pragma unroll
;                 for (int m = 0; m < 4; ++m)
; #pragma unroll
;                     for (int n = 0; n < 2; ++n) acc[a][b][m][n] = (f32x4){0.f, 0.f, 0.f, 0.f};
;         cur = nxt; cA = nA; cB = nB; ++ui;
;         if constexpr (ALIGN_EPI) { if (wr == 1) PG8_BAR; }
	v_mov_b64_e32 v[36:37], v[204:205]
	v_lshlrev_b32_e32 v39, 16, v36
	v_and_b32_e32 v36, 0xffff0000, v36
	v_mul_f32_e32 v30, v30, v39
	v_mul_f32_e32 v31, v31, v36
	v_mul_f32_e32 v30, 0x41800000, v30
	v_mul_f32_e32 v31, 0x41800000, v31
	v_cvt_pk_fp8_f32 v38, v30, v31
	v_lshlrev_b32_e32 v42, 16, v37
	v_and_b32_e32 v37, 0xffff0000, v37
	v_mul_f32_e32 v32, v32, v42
	v_mul_f32_e32 v30, v33, v37
	v_mul_f32_e32 v31, 0x41800000, v32
	v_mul_f32_e32 v30, 0x41800000, v30
	v_cvt_pk_fp8_f32 v38, v31, v30 op_sel:[0,0,1]
	v_lshlrev_b64 v[30:31], 12, v[40:41]
	v_lshl_add_u64 v[30:31], v[126:127], 0, v[30:31]
	v_mov_b32_e32 v36, 0
	global_store_dword v[30:31], v38, off
	s_waitcnt vmcnt(31)
	v_mov_b64_e32 v[32:33], v[206:207]
	v_lshlrev_b32_e32 v37, 16, v32
	v_and_b32_e32 v32, 0xffff0000, v32
	v_mul_f32_e32 v26, v26, v37
	v_mul_f32_e32 v27, v27, v32
	v_mul_f32_e32 v26, 0x41800000, v26
	v_mul_f32_e32 v27, 0x41800000, v27
	v_cvt_pk_fp8_f32 v36, v26, v27
	v_lshlrev_b32_e32 v38, 16, v33
	v_and_b32_e32 v33, 0xffff0000, v33
	v_mul_f32_e32 v28, v28, v38
	v_mul_f32_e32 v26, v29, v33
	v_mul_f32_e32 v27, 0x41800000, v28
	v_mul_f32_e32 v26, 0x41800000, v26
	v_cvt_pk_fp8_f32 v36, v27, v26 op_sel:[0,0,1]
	v_mov_b32_e32 v28, 0
	global_store_dword v[30:31], v36, off offset:16
	s_waitcnt vmcnt(31)
	v_mov_b64_e32 v[26:27], v[208:209]
	v_lshlrev_b32_e32 v29, 16, v26
	v_and_b32_e32 v26, 0xffff0000, v26
	v_mul_f32_e32 v22, v22, v29
	v_mul_f32_e32 v23, v23, v26
	v_mul_f32_e32 v22, 0x41800000, v22
	v_mul_f32_e32 v23, 0x41800000, v23
	v_cvt_pk_fp8_f32 v28, v22, v23
	v_lshlrev_b32_e32 v32, 16, v27
	v_and_b32_e32 v27, 0xffff0000, v27
	v_mul_f32_e32 v24, v24, v32
	v_mul_f32_e32 v22, v25, v27
	v_mul_f32_e32 v23, 0x41800000, v24
	v_mul_f32_e32 v22, 0x41800000, v22
	v_cvt_pk_fp8_f32 v28, v23, v22 op_sel:[0,0,1]
	v_add_u32_e32 v24, 0xb0, v138
	v_ashrrev_i32_e32 v25, 31, v24
	v_lshlrev_b64 v[26:27], 14, v[24:25]
	global_store_dword v[30:31], v28, off offset:128
	s_waitcnt vmcnt(31)
	v_mov_b64_e32 v[22:23], v[210:211]
	v_mov_b32_e32 v28, 0
	v_lshl_add_u64 v[26:27], s[12:13], 0, v[26:27]
	v_lshl_add_u64 v[26:27], v[26:27], 0, v[140:141]
	v_lshlrev_b32_e32 v29, 16, v22
	v_and_b32_e32 v22, 0xffff0000, v22
	v_mul_f32_e32 v18, v18, v29
	v_mul_f32_e32 v19, v19, v22
	v_mul_f32_e32 v18, 0x41800000, v18
	v_mul_f32_e32 v19, 0x41800000, v19
	v_cvt_pk_fp8_f32 v28, v18, v19
	v_lshlrev_b32_e32 v32, 16, v23
	v_and_b32_e32 v23, 0xffff0000, v23
	v_mul_f32_e32 v20, v20, v32
	v_mul_f32_e32 v18, v21, v23
	v_mul_f32_e32 v19, 0x41800000, v20
	v_mul_f32_e32 v18, 0x41800000, v18
	v_cvt_pk_fp8_f32 v28, v19, v18 op_sel:[0,0,1]
	v_add_co_u32_e32 v18, vcc, s66, v26
	v_mov_b32_e32 v22, 0
	global_store_dword v[30:31], v28, off offset:144
	v_addc_co_u32_e32 v19, vcc, 0, v27, vcc
	s_waitcnt vmcnt(31)
	v_mov_b64_e32 v[20:21], v[212:213]
	s_andn2_b64 vcc, exec, s[0:1]
	s_mov_b64 s[0:1], -1
	v_lshlrev_b32_e32 v23, 16, v20
	v_and_b32_e32 v20, 0xffff0000, v20
	v_mul_f32_e32 v14, v14, v23
	v_mul_f32_e32 v15, v15, v20
	v_mul_f32_e32 v14, 0x41800000, v14
	v_mul_f32_e32 v15, 0x41800000, v15
	v_cvt_pk_fp8_f32 v22, v14, v15
	v_lshlrev_b32_e32 v26, 16, v21
	v_and_b32_e32 v21, 0xffff0000, v21
	v_mul_f32_e32 v16, v16, v26
	v_mul_f32_e32 v14, v17, v21
	v_mul_f32_e32 v15, 0x41800000, v16
	v_mul_f32_e32 v14, 0x41800000, v14
	v_cvt_pk_fp8_f32 v22, v15, v14 op_sel:[0,0,1]
	v_lshlrev_b64 v[14:15], 12, v[24:25]
	v_lshl_add_u64 v[14:15], v[126:127], 0, v[14:15]
	v_mov_b32_e32 v20, 0
	global_store_dword v[14:15], v22, off
	s_waitcnt vmcnt(31)
	v_mov_b64_e32 v[16:17], v[214:215]
	v_lshlrev_b32_e32 v21, 16, v16
	v_and_b32_e32 v16, 0xffff0000, v16
	v_mul_f32_e32 v10, v10, v21
	v_mul_f32_e32 v11, v11, v16
	v_mul_f32_e32 v10, 0x41800000, v10
	v_mul_f32_e32 v11, 0x41800000, v11
	v_cvt_pk_fp8_f32 v20, v10, v11
	v_lshlrev_b32_e32 v22, 16, v17
	v_and_b32_e32 v17, 0xffff0000, v17
	v_mul_f32_e32 v12, v12, v22
	v_mul_f32_e32 v10, v13, v17
	v_mul_f32_e32 v11, 0x41800000, v12
	v_mul_f32_e32 v10, 0x41800000, v10
	v_cvt_pk_fp8_f32 v20, v11, v10 op_sel:[0,0,1]
	v_mov_b32_e32 v12, 0
	global_store_dword v[14:15], v20, off offset:16
	s_waitcnt vmcnt(31)
	v_mov_b64_e32 v[10:11], v[216:217]
	v_lshlrev_b32_e32 v13, 16, v10
	v_and_b32_e32 v10, 0xffff0000, v10
	v_mul_f32_e32 v6, v6, v13
	v_mul_f32_e32 v7, v7, v10
	v_mul_f32_e32 v6, 0x41800000, v6
	v_mul_f32_e32 v7, 0x41800000, v7
	v_cvt_pk_fp8_f32 v12, v6, v7
	v_lshlrev_b32_e32 v16, 16, v11
	v_and_b32_e32 v11, 0xffff0000, v11
	v_mul_f32_e32 v8, v8, v16
	v_mul_f32_e32 v6, v9, v11
	v_mul_f32_e32 v7, 0x41800000, v8
	v_mul_f32_e32 v6, 0x41800000, v6
	v_cvt_pk_fp8_f32 v12, v7, v6 op_sel:[0,0,1]
	v_mov_b32_e32 v8, 0
	global_store_dword v[14:15], v12, off offset:128
	s_waitcnt vmcnt(31)
	v_mov_b64_e32 v[6:7], v[218:219]
	v_lshlrev_b32_e32 v9, 16, v6
	v_and_b32_e32 v6, 0xffff0000, v6
	v_mul_f32_e32 v2, v2, v9
	v_mul_f32_e32 v3, v3, v6
	v_mul_f32_e32 v2, 0x41800000, v2
	v_mul_f32_e32 v3, 0x41800000, v3
	v_cvt_pk_fp8_f32 v8, v2, v3
	v_lshlrev_b32_e32 v10, 16, v7
	v_and_b32_e32 v7, 0xffff0000, v7
	v_mul_f32_e32 v4, v4, v10
	v_mul_f32_e32 v2, v5, v7
	v_mul_f32_e32 v3, 0x41800000, v4
	v_mul_f32_e32 v2, 0x41800000, v2
	v_cvt_pk_fp8_f32 v8, v3, v2 op_sel:[0,0,1]
	global_store_dword v[14:15], v8, off offset:144
	s_cbranch_vccnz .LBB0_2981
	s_andn2_b64 vcc, exec, s[10:11]
	s_cbranch_vccnz .LBB0_2980
	s_barrier
	s_branch .LBB0_2980
